# v15 + hand-written attention epilogues: O/l to bf16 through a wave-private LDS image, eight 16-byte whole-row stores per wave instead of 32 dword stores
# baseline (speedup 1.0000x reference)
.Lattn_prio_done:
	s_add_u32 s28, s60, 0x4000
	s_addc_u32 s29, s61, 0
	s_lshl_b64 s[0:1], s[6:7], 2
	s_add_u32 s46, s28, s0
	s_addc_u32 s47, s29, s1
	s_and_b64 s[2:3], s[36:37], exec
	s_movk_i32 s2, 0x120
	s_cselect_b32 s52, s2, 0x100
	s_add_u32 s53, s60, 0x56190000
	s_addc_u32 s54, s61, 0
	s_add_u32 s55, s60, 0x54690000
	s_addc_u32 s56, s61, 0
	s_branch .LBB0_6672
.LBB0_6670:
	s_mov_b64 s[4:5], 0

.LBB0_6719:
	v_and_b32_e32 v68, 0x3fffffc0, v0
	s_mov_b32 s4, 0x18000
	v_lshl_add_u32 v68, v68, 2, s4
	v_bfe_u32 v84, v0, 5, 1
	v_cmp_eq_u32_e32 vcc, 0, v84
	s_and_saveexec_b64 s[40:41], vcc
	v_and_b32_e32 v69, 31, v0
	v_lshl_add_u32 v69, v69, 2, v68
	ds_write_b32 v69, v203
	s_or_b64 exec, exec, s[40:41]
	s_waitcnt lgkmcnt(0)
	v_lshl_add_u32 v68, v84, 4, v68
	ds_read_b128 v[80:83], v68
	ds_read_b128 v[76:79], v68 offset:32
	ds_read_b128 v[72:75], v68 offset:64
	ds_read_b128 v[68:71], v68 offset:96
	v_readfirstlane_b32 s4, v0
	s_nop 3
	s_lshr_b32 s4, s4, 6
	s_lshl_b64 s[2:3], s[48:49], 12
	s_add_u32 s2, s60, s2
	s_addc_u32 s3, s61, s3
	s_lshl_b32 s5, s6, 8
	s_add_u32 s2, s2, s5
	s_addc_u32 s3, s3, 0
	s_add_u32 s2, s2, 0x5c490c00
	s_addc_u32 s3, s3, 0
	s_lshl_b32 s5, s4, 17
	s_add_u32 s2, s2, s5
	s_addc_u32 s3, s3, 0
	s_mul_i32 s5, s4, 0x2200
	s_add_i32 s5, s5, 0x0
	v_and_b32_e32 v88, 31, v0
	v_lshl_add_u32 v85, v88, 1, s5
	s_movk_i32 s4, 0x440
	v_mul_u32_u24_e32 v88, s4, v84
	v_add_u32_e32 v85, v85, v88
	v_bfe_u32 v88, v0, 4, 2
	v_and_b32_e32 v2, 15, v0
	s_movk_i32 s4, 0x110
	v_mul_u32_u24_e32 v86, s4, v88
	v_lshl_add_u32 v86, v2, 4, v86
	v_add_u32_e32 v86, s5, v86
	v_lshlrev_b32_e32 v87, 12, v88
	v_lshl_add_u32 v87, v2, 4, v87
	s_waitcnt lgkmcnt(0)
	v_rcp_f32_e32 v80, v80
	v_rcp_f32_e32 v81, v81
	v_rcp_f32_e32 v82, v82
	v_rcp_f32_e32 v83, v83
	v_rcp_f32_e32 v76, v76
	v_rcp_f32_e32 v77, v77
	v_rcp_f32_e32 v78, v78
	v_rcp_f32_e32 v79, v79
	v_rcp_f32_e32 v72, v72
	v_rcp_f32_e32 v73, v73
	v_rcp_f32_e32 v74, v74
	v_rcp_f32_e32 v75, v75
	v_rcp_f32_e32 v68, v68
	v_rcp_f32_e32 v69, v69
	v_rcp_f32_e32 v70, v70
	v_rcp_f32_e32 v71, v71
	v_mul_f32_e32 v52, v52, v80
	v_mul_f32_e32 v53, v53, v81
	v_cvt_pk_bf16_f32 v52, v52, v53
	ds_write_b16 v85, v52 offset:0
	ds_write_b16_d16_hi v85, v52 offset:272
	v_mul_f32_e32 v54, v54, v82
	v_mul_f32_e32 v55, v55, v83
	v_cvt_pk_bf16_f32 v54, v54, v55
	ds_write_b16 v85, v54 offset:544
	ds_write_b16_d16_hi v85, v54 offset:816
	v_mul_f32_e32 v56, v56, v76
	v_mul_f32_e32 v57, v57, v77
	v_cvt_pk_bf16_f32 v56, v56, v57
	ds_write_b16 v85, v56 offset:2176
	ds_write_b16_d16_hi v85, v56 offset:2448
	v_mul_f32_e32 v58, v58, v78
	v_mul_f32_e32 v59, v59, v79
	v_cvt_pk_bf16_f32 v58, v58, v59
	ds_write_b16 v85, v58 offset:2720
	ds_write_b16_d16_hi v85, v58 offset:2992
	v_mul_f32_e32 v60, v60, v72
	v_mul_f32_e32 v61, v61, v73
	v_cvt_pk_bf16_f32 v60, v60, v61
	ds_write_b16 v85, v60 offset:4352
	ds_write_b16_d16_hi v85, v60 offset:4624
	v_mul_f32_e32 v62, v62, v74
	v_mul_f32_e32 v63, v63, v75
	v_cvt_pk_bf16_f32 v62, v62, v63
	ds_write_b16 v85, v62 offset:4896
	ds_write_b16_d16_hi v85, v62 offset:5168
	v_mul_f32_e32 v64, v64, v68
	v_mul_f32_e32 v65, v65, v69
	v_cvt_pk_bf16_f32 v64, v64, v65
	ds_write_b16 v85, v64 offset:6528
	ds_write_b16_d16_hi v85, v64 offset:6800
	v_mul_f32_e32 v66, v66, v70
	v_mul_f32_e32 v67, v67, v71
	v_cvt_pk_bf16_f32 v66, v66, v67
	ds_write_b16 v85, v66 offset:7072
	ds_write_b16_d16_hi v85, v66 offset:7344
	v_mul_f32_e32 v36, v36, v80
	v_mul_f32_e32 v37, v37, v81
	v_cvt_pk_bf16_f32 v36, v36, v37
	ds_write_b16 v85, v36 offset:64
	ds_write_b16_d16_hi v85, v36 offset:336
	v_mul_f32_e32 v38, v38, v82
	v_mul_f32_e32 v39, v39, v83
	v_cvt_pk_bf16_f32 v38, v38, v39
	ds_write_b16 v85, v38 offset:608
	ds_write_b16_d16_hi v85, v38 offset:880
	v_mul_f32_e32 v40, v40, v76
	v_mul_f32_e32 v41, v41, v77
	v_cvt_pk_bf16_f32 v40, v40, v41
	ds_write_b16 v85, v40 offset:2240
	ds_write_b16_d16_hi v85, v40 offset:2512
	v_mul_f32_e32 v42, v42, v78
	v_mul_f32_e32 v43, v43, v79
	v_cvt_pk_bf16_f32 v42, v42, v43
	ds_write_b16 v85, v42 offset:2784
	ds_write_b16_d16_hi v85, v42 offset:3056
	v_mul_f32_e32 v44, v44, v72
	v_mul_f32_e32 v45, v45, v73
	v_cvt_pk_bf16_f32 v44, v44, v45
	ds_write_b16 v85, v44 offset:4416
	ds_write_b16_d16_hi v85, v44 offset:4688
	v_mul_f32_e32 v46, v46, v74
	v_mul_f32_e32 v47, v47, v75
	v_cvt_pk_bf16_f32 v46, v46, v47
	ds_write_b16 v85, v46 offset:4960
	ds_write_b16_d16_hi v85, v46 offset:5232
	v_mul_f32_e32 v48, v48, v68
	v_mul_f32_e32 v49, v49, v69
	v_cvt_pk_bf16_f32 v48, v48, v49
	ds_write_b16 v85, v48 offset:6592
	ds_write_b16_d16_hi v85, v48 offset:6864
	v_mul_f32_e32 v50, v50, v70
	v_mul_f32_e32 v51, v51, v71
	v_cvt_pk_bf16_f32 v50, v50, v51
	ds_write_b16 v85, v50 offset:7136
	ds_write_b16_d16_hi v85, v50 offset:7408
	v_mul_f32_e32 v20, v20, v80
	v_mul_f32_e32 v21, v21, v81
	v_cvt_pk_bf16_f32 v20, v20, v21
	ds_write_b16 v85, v20 offset:128
	ds_write_b16_d16_hi v85, v20 offset:400
	v_mul_f32_e32 v22, v22, v82
	v_mul_f32_e32 v23, v23, v83
	v_cvt_pk_bf16_f32 v22, v22, v23
	ds_write_b16 v85, v22 offset:672
	ds_write_b16_d16_hi v85, v22 offset:944
	v_mul_f32_e32 v24, v24, v76
	v_mul_f32_e32 v25, v25, v77
	v_cvt_pk_bf16_f32 v24, v24, v25
	ds_write_b16 v85, v24 offset:2304
	ds_write_b16_d16_hi v85, v24 offset:2576
	v_mul_f32_e32 v26, v26, v78
	v_mul_f32_e32 v27, v27, v79
	v_cvt_pk_bf16_f32 v26, v26, v27
	ds_write_b16 v85, v26 offset:2848
	ds_write_b16_d16_hi v85, v26 offset:3120
	v_mul_f32_e32 v28, v28, v72
	v_mul_f32_e32 v29, v29, v73
	v_cvt_pk_bf16_f32 v28, v28, v29
	ds_write_b16 v85, v28 offset:4480
	ds_write_b16_d16_hi v85, v28 offset:4752
	v_mul_f32_e32 v30, v30, v74
	v_mul_f32_e32 v31, v31, v75
	v_cvt_pk_bf16_f32 v30, v30, v31
	ds_write_b16 v85, v30 offset:5024
	ds_write_b16_d16_hi v85, v30 offset:5296
	v_mul_f32_e32 v32, v32, v68
	v_mul_f32_e32 v33, v33, v69
	v_cvt_pk_bf16_f32 v32, v32, v33
	ds_write_b16 v85, v32 offset:6656
	ds_write_b16_d16_hi v85, v32 offset:6928
	v_mul_f32_e32 v34, v34, v70
	v_mul_f32_e32 v35, v35, v71
	v_cvt_pk_bf16_f32 v34, v34, v35
	ds_write_b16 v85, v34 offset:7200
	ds_write_b16_d16_hi v85, v34 offset:7472
	v_mul_f32_e32 v4, v4, v80
	v_mul_f32_e32 v5, v5, v81
	v_cvt_pk_bf16_f32 v4, v4, v5
	ds_write_b16 v85, v4 offset:192
	ds_write_b16_d16_hi v85, v4 offset:464
	v_mul_f32_e32 v6, v6, v82
	v_mul_f32_e32 v7, v7, v83
	v_cvt_pk_bf16_f32 v6, v6, v7
	ds_write_b16 v85, v6 offset:736
	ds_write_b16_d16_hi v85, v6 offset:1008
	v_mul_f32_e32 v8, v8, v76
	v_mul_f32_e32 v9, v9, v77
	v_cvt_pk_bf16_f32 v8, v8, v9
	ds_write_b16 v85, v8 offset:2368
	ds_write_b16_d16_hi v85, v8 offset:2640
	v_mul_f32_e32 v10, v10, v78
	v_mul_f32_e32 v11, v11, v79
	v_cvt_pk_bf16_f32 v10, v10, v11
	ds_write_b16 v85, v10 offset:2912
	ds_write_b16_d16_hi v85, v10 offset:3184
	v_mul_f32_e32 v12, v12, v72
	v_mul_f32_e32 v13, v13, v73
	v_cvt_pk_bf16_f32 v12, v12, v13
	ds_write_b16 v85, v12 offset:4544
	ds_write_b16_d16_hi v85, v12 offset:4816
	v_mul_f32_e32 v14, v14, v74
	v_mul_f32_e32 v15, v15, v75
	v_cvt_pk_bf16_f32 v14, v14, v15
	ds_write_b16 v85, v14 offset:5088
	ds_write_b16_d16_hi v85, v14 offset:5360
	v_mul_f32_e32 v16, v16, v68
	v_mul_f32_e32 v17, v17, v69
	v_cvt_pk_bf16_f32 v16, v16, v17
	ds_write_b16 v85, v16 offset:6720
	ds_write_b16_d16_hi v85, v16 offset:6992
	v_mul_f32_e32 v18, v18, v70
	v_mul_f32_e32 v19, v19, v71
	v_cvt_pk_bf16_f32 v18, v18, v19
	ds_write_b16 v85, v18 offset:7264
	ds_write_b16_d16_hi v85, v18 offset:7536
	s_waitcnt lgkmcnt(0)
	ds_read_b128 v[4:7], v86 offset:0
	ds_read_b128 v[8:11], v86 offset:1088
	ds_read_b128 v[12:15], v86 offset:2176
	ds_read_b128 v[16:19], v86 offset:3264
	ds_read_b128 v[20:23], v86 offset:4352
	ds_read_b128 v[24:27], v86 offset:5440
	ds_read_b128 v[28:31], v86 offset:6528
	ds_read_b128 v[32:35], v86 offset:7616
	s_waitcnt lgkmcnt(7)
	global_store_dwordx4 v87, v[4:7], s[2:3]
	s_add_u32 s2, s2, 0x4000
	s_addc_u32 s3, s3, 0
	s_waitcnt lgkmcnt(6)
	global_store_dwordx4 v87, v[8:11], s[2:3]
	s_add_u32 s2, s2, 0x4000
	s_addc_u32 s3, s3, 0
	s_waitcnt lgkmcnt(5)
	global_store_dwordx4 v87, v[12:15], s[2:3]
	s_add_u32 s2, s2, 0x4000
	s_addc_u32 s3, s3, 0
	s_waitcnt lgkmcnt(4)
	global_store_dwordx4 v87, v[16:19], s[2:3]
	s_add_u32 s2, s2, 0x4000
	s_addc_u32 s3, s3, 0
	s_waitcnt lgkmcnt(3)
	global_store_dwordx4 v87, v[20:23], s[2:3]
	s_add_u32 s2, s2, 0x4000
	s_addc_u32 s3, s3, 0
	s_waitcnt lgkmcnt(2)
	global_store_dwordx4 v87, v[24:27], s[2:3]
	s_add_u32 s2, s2, 0x4000
	s_addc_u32 s3, s3, 0
	s_waitcnt lgkmcnt(1)
	global_store_dwordx4 v87, v[28:31], s[2:3]
	s_add_u32 s2, s2, 0x4000
	s_addc_u32 s3, s3, 0
	s_waitcnt lgkmcnt(0)
	global_store_dwordx4 v87, v[32:35], s[2:3]
	s_nop 1
	s_branch .LBB0_6670
.LBB0_6849:
	v_max_f32_e32 v2, v201, v201
	v_max_f32_e32 v1, v1, v1
	v_max_f32_e32 v1, v1, v2
	v_max_f32_e32 v2, v200, v200
	s_nop 1
	v_max_f32_e32 v4, v199, v199
	v_mul_f32_e32 v1, 0x418293ee, v1
	v_max_f32_e32 v2, v4, v2
	v_mul_f32_e32 v1, v2, v1
	s_mov_b32 s2, 0x42c00000
	v_cmp_ngt_f32_e32 vcc, s2, v1
	s_ashr_i32 s50, s62, 6
	v_lshlrev_b32_e32 v2, 4, v197
	v_cndmask_b32_e64 v1, 0, 1, vcc
	s_waitcnt vmcnt(4)
	v_ashrrev_i32_e32 v168, 3, v197
	v_readfirstlane_b32 s2, v1
	s_bitcmp1_b32 s2, 0
	s_cselect_b64 s[2:3], -1, 0
	s_xor_b64 s[44:45], s[2:3], -1
	s_add_u32 s0, s60, s0
	s_addc_u32 s1, s61, s1
	s_add_u32 s46, s0, 0x4100
	s_addc_u32 s47, s1, 0
	s_and_b64 s[0:1], s[36:37], exec
	s_movk_i32 s0, 0x240
	s_cselect_b32 s51, s0, 0x200
	s_movk_i32 s0, 0x5b4
	s_cselect_b32 s52, s0, 0xc06
	s_add_i32 s53, s51, 0x48
	v_readlane_b32 s0, v252, 55
	s_add_i32 s54, s53, s0
	s_and_b64 s[0:1], s[36:37], exec
	s_movk_i32 s0, 0xfd78
	s_cselect_b32 s55, s0, 0xfffffdb8
	s_add_u32 s9, s60, 0x23c90000
	s_addc_u32 s57, s61, 0
	s_add_u32 s58, s60, 0x3c90000
	s_addc_u32 s59, s61, 0
	s_add_u32 s62, s60, 0x3b90000
	s_addc_u32 s63, s61, 0
	s_add_u32 s85, s60, 0x3a10000
	s_addc_u32 s86, s61, 0
	v_lshlrev_b32_e32 v1, 2, v197
	s_add_u32 s87, s60, 0x2a10000
	v_and_b32_e32 v4, 0x70, v2
	s_movk_i32 s0, 0x108
	v_ashrrev_i32_e32 v2, 1, v197
	v_and_b32_e32 v171, 60, v1
	s_addc_u32 s88, s61, 0
	v_and_b32_e32 v8, -8, v2
	v_mul_lo_u32 v2, v168, s0
	s_add_u32 s89, s60, 0x610000
	v_mad_u32_u24 v5, v171, s0, 0
	v_add_u32_e32 v9, 0, v2
	v_lshlrev_b32_e32 v2, 5, v197
	v_readlane_b32 s0, v255, 20
	s_addc_u32 s90, s61, 0
	v_and_b32_e32 v10, 0xe0, v2
	v_readlane_b32 s1, v255, 21
	s_mov_b32 s2, s0
	s_lshl_b32 s0, s0, 3
	v_lshlrev_b32_e32 v2, 4, v198
	s_or_b32 s84, s0, 32
	v_lshl_add_u64 v[6:7], s[60:61], 0, v[2:3]
	s_mov_b64 s[0:1], 0x57c90000
	s_waitcnt vmcnt(3)
	v_lshl_add_u64 v[174:175], v[6:7], 0, s[0:1]
	s_mov_b64 s[0:1], 0x5a090000
	s_lshl_b32 s6, s2, 9
	s_waitcnt vmcnt(2)
	v_lshl_add_u64 v[176:177], v[6:7], 0, s[0:1]
	s_add_u32 s0, s60, 0x5c490000
	s_addc_u32 s1, s61, 0
	s_add_u32 s91, s60, 0x4e390000
	s_addc_u32 s8, s61, 0
	s_add_u32 s97, s60, 0x4bf90000
	v_readlane_b32 s64, v251, 5
	v_lshl_add_u64 v[178:179], s[0:1], 0, v[2:3]
	s_addc_u32 s56, s61, 0
	s_lshl_b64 s[0:1], s[6:7], 2
	v_readlane_b32 s68, v251, 9
	v_ashrrev_i32_e32 v1, 2, v197
	v_readlane_b32 s69, v251, 10
	s_add_u32 s0, s68, s0
	v_and_b32_e32 v170, -4, v1
	s_addc_u32 s1, s69, s1
	v_lshlrev_b32_e32 v2, 5, v198
	v_ashrrev_i32_e32 v1, 31, v170
	v_ashrrev_i32_e32 v169, 31, v168
	v_lshlrev_b32_e32 v172, 3, v198
	s_waitcnt vmcnt(1)
	v_lshl_add_u64 v[180:181], s[0:1], 0, v[2:3]
	v_lshlrev_b32_e32 v182, 1, v4
	v_add_u32_e32 v173, v5, v8
	s_waitcnt vmcnt(0)
	v_add_u32_e32 v184, v9, v10
	v_readlane_b32 s65, v251, 6
	v_readlane_b32 s66, v251, 7
	v_readlane_b32 s67, v251, 8
	v_readlane_b32 s70, v251, 11
	v_readlane_b32 s71, v251, 12
	v_readlane_b32 s72, v251, 13
	v_readlane_b32 s73, v251, 14
	v_readlane_b32 s74, v251, 15
	v_readlane_b32 s75, v251, 16
	v_readlane_b32 s76, v251, 17
	v_readlane_b32 s77, v251, 18
	v_readlane_b32 s78, v251, 19
	v_readlane_b32 s79, v251, 20
	s_branch .LBB0_6853
.LBB0_6851:
	s_mov_b64 s[0:1], 0

.LBB0_6943:
	v_and_b32_e32 v68, 0x3fffffc0, v0
	s_mov_b32 s2, 0x10000
	v_lshl_add_u32 v68, v68, 2, s2
	v_bfe_u32 v84, v0, 5, 1
	v_cmp_eq_u32_e32 vcc, 0, v84
	s_and_saveexec_b64 s[4:5], vcc
	v_and_b32_e32 v69, 31, v0
	v_lshl_add_u32 v69, v69, 2, v68
	ds_write_b32 v69, v185
	s_or_b64 exec, exec, s[4:5]
	s_waitcnt lgkmcnt(0)
	v_lshl_add_u32 v68, v84, 4, v68
	ds_read_b128 v[80:83], v68
	ds_read_b128 v[76:79], v68 offset:32
	ds_read_b128 v[72:75], v68 offset:64
	ds_read_b128 v[68:71], v68 offset:96
	v_readfirstlane_b32 s2, v0
	s_nop 3
	s_lshr_b32 s2, s2, 6
	s_lshl_b64 s[0:1], s[0:1], 12
	s_add_u32 s0, s60, s0
	s_addc_u32 s1, s61, s1
	s_lshl_b32 s3, s6, 1
	s_add_u32 s0, s0, s3
	s_addc_u32 s1, s1, 0
	s_add_u32 s0, s0, 0x5c490400
	s_addc_u32 s1, s1, 0
	s_lshl_b32 s3, s2, 17
	s_add_u32 s0, s0, s3
	s_addc_u32 s1, s1, 0
	s_mul_i32 s3, s2, 0x2200
	s_add_i32 s3, s3, 0x10800
	v_and_b32_e32 v88, 31, v0
	v_lshl_add_u32 v85, v88, 1, s3
	s_movk_i32 s2, 0x440
	v_mul_u32_u24_e32 v88, s2, v84
	v_add_u32_e32 v85, v85, v88
	v_bfe_u32 v88, v0, 4, 2
	v_and_b32_e32 v2, 15, v0
	s_movk_i32 s2, 0x110
	v_mul_u32_u24_e32 v86, s2, v88
	v_lshl_add_u32 v86, v2, 4, v86
	v_add_u32_e32 v86, s3, v86
	v_lshlrev_b32_e32 v87, 12, v88
	v_lshl_add_u32 v87, v2, 4, v87
	s_waitcnt lgkmcnt(0)
	v_rcp_f32_e32 v80, v80
	v_rcp_f32_e32 v81, v81
	v_rcp_f32_e32 v82, v82
	v_rcp_f32_e32 v83, v83
	v_rcp_f32_e32 v76, v76
	v_rcp_f32_e32 v77, v77
	v_rcp_f32_e32 v78, v78
	v_rcp_f32_e32 v79, v79
	v_rcp_f32_e32 v72, v72
	v_rcp_f32_e32 v73, v73
	v_rcp_f32_e32 v74, v74
	v_rcp_f32_e32 v75, v75
	v_rcp_f32_e32 v68, v68
	v_rcp_f32_e32 v69, v69
	v_rcp_f32_e32 v70, v70
	v_rcp_f32_e32 v71, v71
	v_mul_f32_e32 v52, v52, v80
	v_mul_f32_e32 v53, v53, v81
	v_cvt_pk_bf16_f32 v52, v52, v53
	ds_write_b16 v85, v52 offset:0
	ds_write_b16_d16_hi v85, v52 offset:272
	v_mul_f32_e32 v54, v54, v82
	v_mul_f32_e32 v55, v55, v83
	v_cvt_pk_bf16_f32 v54, v54, v55
	ds_write_b16 v85, v54 offset:544
	ds_write_b16_d16_hi v85, v54 offset:816
	v_mul_f32_e32 v56, v56, v76
	v_mul_f32_e32 v57, v57, v77
	v_cvt_pk_bf16_f32 v56, v56, v57
	ds_write_b16 v85, v56 offset:2176
	ds_write_b16_d16_hi v85, v56 offset:2448
	v_mul_f32_e32 v58, v58, v78
	v_mul_f32_e32 v59, v59, v79
	v_cvt_pk_bf16_f32 v58, v58, v59
	ds_write_b16 v85, v58 offset:2720
	ds_write_b16_d16_hi v85, v58 offset:2992
	v_mul_f32_e32 v60, v60, v72
	v_mul_f32_e32 v61, v61, v73
	v_cvt_pk_bf16_f32 v60, v60, v61
	ds_write_b16 v85, v60 offset:4352
	ds_write_b16_d16_hi v85, v60 offset:4624
	v_mul_f32_e32 v62, v62, v74
	v_mul_f32_e32 v63, v63, v75
	v_cvt_pk_bf16_f32 v62, v62, v63
	ds_write_b16 v85, v62 offset:4896
	ds_write_b16_d16_hi v85, v62 offset:5168
	v_mul_f32_e32 v64, v64, v68
	v_mul_f32_e32 v65, v65, v69
	v_cvt_pk_bf16_f32 v64, v64, v65
	ds_write_b16 v85, v64 offset:6528
	ds_write_b16_d16_hi v85, v64 offset:6800
	v_mul_f32_e32 v66, v66, v70
	v_mul_f32_e32 v67, v67, v71
	v_cvt_pk_bf16_f32 v66, v66, v67
	ds_write_b16 v85, v66 offset:7072
	ds_write_b16_d16_hi v85, v66 offset:7344
	v_mul_f32_e32 v36, v36, v80
	v_mul_f32_e32 v37, v37, v81
	v_cvt_pk_bf16_f32 v36, v36, v37
	ds_write_b16 v85, v36 offset:64
	ds_write_b16_d16_hi v85, v36 offset:336
	v_mul_f32_e32 v38, v38, v82
	v_mul_f32_e32 v39, v39, v83
	v_cvt_pk_bf16_f32 v38, v38, v39
	ds_write_b16 v85, v38 offset:608
	ds_write_b16_d16_hi v85, v38 offset:880
	v_mul_f32_e32 v40, v40, v76
	v_mul_f32_e32 v41, v41, v77
	v_cvt_pk_bf16_f32 v40, v40, v41
	ds_write_b16 v85, v40 offset:2240
	ds_write_b16_d16_hi v85, v40 offset:2512
	v_mul_f32_e32 v42, v42, v78
	v_mul_f32_e32 v43, v43, v79
	v_cvt_pk_bf16_f32 v42, v42, v43
	ds_write_b16 v85, v42 offset:2784
	ds_write_b16_d16_hi v85, v42 offset:3056
	v_mul_f32_e32 v44, v44, v72
	v_mul_f32_e32 v45, v45, v73
	v_cvt_pk_bf16_f32 v44, v44, v45
	ds_write_b16 v85, v44 offset:4416
	ds_write_b16_d16_hi v85, v44 offset:4688
	v_mul_f32_e32 v46, v46, v74
	v_mul_f32_e32 v47, v47, v75
	v_cvt_pk_bf16_f32 v46, v46, v47
	ds_write_b16 v85, v46 offset:4960
	ds_write_b16_d16_hi v85, v46 offset:5232
	v_mul_f32_e32 v48, v48, v68
	v_mul_f32_e32 v49, v49, v69
	v_cvt_pk_bf16_f32 v48, v48, v49
	ds_write_b16 v85, v48 offset:6592
	ds_write_b16_d16_hi v85, v48 offset:6864
	v_mul_f32_e32 v50, v50, v70
	v_mul_f32_e32 v51, v51, v71
	v_cvt_pk_bf16_f32 v50, v50, v51
	ds_write_b16 v85, v50 offset:7136
	ds_write_b16_d16_hi v85, v50 offset:7408
	v_mul_f32_e32 v20, v20, v80
	v_mul_f32_e32 v21, v21, v81
	v_cvt_pk_bf16_f32 v20, v20, v21
	ds_write_b16 v85, v20 offset:128
	ds_write_b16_d16_hi v85, v20 offset:400
	v_mul_f32_e32 v22, v22, v82
	v_mul_f32_e32 v23, v23, v83
	v_cvt_pk_bf16_f32 v22, v22, v23
	ds_write_b16 v85, v22 offset:672
	ds_write_b16_d16_hi v85, v22 offset:944
	v_mul_f32_e32 v24, v24, v76
	v_mul_f32_e32 v25, v25, v77
	v_cvt_pk_bf16_f32 v24, v24, v25
	ds_write_b16 v85, v24 offset:2304
	ds_write_b16_d16_hi v85, v24 offset:2576
	v_mul_f32_e32 v26, v26, v78
	v_mul_f32_e32 v27, v27, v79
	v_cvt_pk_bf16_f32 v26, v26, v27
	ds_write_b16 v85, v26 offset:2848
	ds_write_b16_d16_hi v85, v26 offset:3120
	v_mul_f32_e32 v28, v28, v72
	v_mul_f32_e32 v29, v29, v73
	v_cvt_pk_bf16_f32 v28, v28, v29
	ds_write_b16 v85, v28 offset:4480
	ds_write_b16_d16_hi v85, v28 offset:4752
	v_mul_f32_e32 v30, v30, v74
	v_mul_f32_e32 v31, v31, v75
	v_cvt_pk_bf16_f32 v30, v30, v31
	ds_write_b16 v85, v30 offset:5024
	ds_write_b16_d16_hi v85, v30 offset:5296
	v_mul_f32_e32 v32, v32, v68
	v_mul_f32_e32 v33, v33, v69
	v_cvt_pk_bf16_f32 v32, v32, v33
	ds_write_b16 v85, v32 offset:6656
	ds_write_b16_d16_hi v85, v32 offset:6928
	v_mul_f32_e32 v34, v34, v70
	v_mul_f32_e32 v35, v35, v71
	v_cvt_pk_bf16_f32 v34, v34, v35
	ds_write_b16 v85, v34 offset:7200
	ds_write_b16_d16_hi v85, v34 offset:7472
	v_mul_f32_e32 v4, v4, v80
	v_mul_f32_e32 v5, v5, v81
	v_cvt_pk_bf16_f32 v4, v4, v5
	ds_write_b16 v85, v4 offset:192
	ds_write_b16_d16_hi v85, v4 offset:464
	v_mul_f32_e32 v6, v6, v82
	v_mul_f32_e32 v7, v7, v83
	v_cvt_pk_bf16_f32 v6, v6, v7
	ds_write_b16 v85, v6 offset:736
	ds_write_b16_d16_hi v85, v6 offset:1008
	v_mul_f32_e32 v8, v8, v76
	v_mul_f32_e32 v9, v9, v77
	v_cvt_pk_bf16_f32 v8, v8, v9
	ds_write_b16 v85, v8 offset:2368
	ds_write_b16_d16_hi v85, v8 offset:2640
	v_mul_f32_e32 v10, v10, v78
	v_mul_f32_e32 v11, v11, v79
	v_cvt_pk_bf16_f32 v10, v10, v11
	ds_write_b16 v85, v10 offset:2912
	ds_write_b16_d16_hi v85, v10 offset:3184
	v_mul_f32_e32 v12, v12, v72
	v_mul_f32_e32 v13, v13, v73
	v_cvt_pk_bf16_f32 v12, v12, v13
	ds_write_b16 v85, v12 offset:4544
	ds_write_b16_d16_hi v85, v12 offset:4816
	v_mul_f32_e32 v14, v14, v74
	v_mul_f32_e32 v15, v15, v75
	v_cvt_pk_bf16_f32 v14, v14, v15
	ds_write_b16 v85, v14 offset:5088
	ds_write_b16_d16_hi v85, v14 offset:5360
	v_mul_f32_e32 v16, v16, v68
	v_mul_f32_e32 v17, v17, v69
	v_cvt_pk_bf16_f32 v16, v16, v17
	ds_write_b16 v85, v16 offset:6720
	ds_write_b16_d16_hi v85, v16 offset:6992
	v_mul_f32_e32 v18, v18, v70
	v_mul_f32_e32 v19, v19, v71
	v_cvt_pk_bf16_f32 v18, v18, v19
	ds_write_b16 v85, v18 offset:7264
	ds_write_b16_d16_hi v85, v18 offset:7536
	s_waitcnt lgkmcnt(0)
	ds_read_b128 v[4:7], v86 offset:0
	ds_read_b128 v[8:11], v86 offset:1088
	ds_read_b128 v[12:15], v86 offset:2176
	ds_read_b128 v[16:19], v86 offset:3264
	ds_read_b128 v[20:23], v86 offset:4352
	ds_read_b128 v[24:27], v86 offset:5440
	ds_read_b128 v[28:31], v86 offset:6528
	ds_read_b128 v[32:35], v86 offset:7616
	s_waitcnt lgkmcnt(7)
	global_store_dwordx4 v87, v[4:7], s[0:1]
	s_add_u32 s0, s0, 0x4000
	s_addc_u32 s1, s1, 0
	s_waitcnt lgkmcnt(6)
	global_store_dwordx4 v87, v[8:11], s[0:1]
	s_add_u32 s0, s0, 0x4000
	s_addc_u32 s1, s1, 0
	s_waitcnt lgkmcnt(5)
	global_store_dwordx4 v87, v[12:15], s[0:1]
	s_add_u32 s0, s0, 0x4000
	s_addc_u32 s1, s1, 0
	s_waitcnt lgkmcnt(4)
	global_store_dwordx4 v87, v[16:19], s[0:1]
	s_add_u32 s0, s0, 0x4000
	s_addc_u32 s1, s1, 0
	s_waitcnt lgkmcnt(3)
	global_store_dwordx4 v87, v[20:23], s[0:1]
	s_add_u32 s0, s0, 0x4000
	s_addc_u32 s1, s1, 0
	s_waitcnt lgkmcnt(2)
	global_store_dwordx4 v87, v[24:27], s[0:1]
	s_add_u32 s0, s0, 0x4000
	s_addc_u32 s1, s1, 0
	s_waitcnt lgkmcnt(1)
	global_store_dwordx4 v87, v[28:31], s[0:1]
	s_add_u32 s0, s0, 0x4000
	s_addc_u32 s1, s1, 0
	s_waitcnt lgkmcnt(0)
	global_store_dwordx4 v87, v[32:35], s[0:1]
	s_nop 1
	s_branch .LBB0_6851
